# packed f32 ops next to MFMAs split into scalar pairs: attention tile-loop rescale (16) and scan state decay / v-prime (44)
# speedup vs baseline: 1.0019x; 1.0019x over previous
.LBB0_670:
	v_max_f32_e32 v130, v51, v51
	v_max_f32_e32 v180, v50, v50
	v_max_f32_e32 v130, v180, v130
	v_max3_f32 v130, v130, v52, v53
	v_max3_f32 v130, v130, v54, v55
	v_max3_f32 v130, v130, v56, v57
	v_max3_f32 v130, v130, v58, v59
	v_max3_f32 v130, v130, v60, v61
	v_max3_f32 v130, v130, v62, v63
	v_max3_f32 v130, v130, v64, v65
	v_max3_f32 v130, v130, v34, v35
	v_max3_f32 v130, v130, v36, v37
	v_max3_f32 v130, v130, v38, v39
	v_max3_f32 v130, v130, v40, v41
	v_max3_f32 v130, v130, v42, v43
	v_max3_f32 v130, v130, v44, v45
	v_max3_f32 v130, v130, v46, v47
	v_max3_f32 v130, v130, v48, v49
	v_mov_b32_e32 v180, v130
	v_mov_b32_e32 v181, v130
	s_nop 1
	v_permlane32_swap_b32_e32 v180, v181
	v_cndmask_b32_e64 v180, v180, v181, s[2:3]
	v_max3_f32 v130, v179, v130, v180
	v_sub_f32_e32 v50, v50, v130
	v_exp_f32_e32 v50, v50
	v_sub_f32_e32 v51, v51, v130
	v_exp_f32_e32 v51, v51
	v_sub_f32_e32 v52, v52, v130
	v_exp_f32_e32 v52, v52
	v_sub_f32_e32 v53, v53, v130
	v_exp_f32_e32 v53, v53
	v_sub_f32_e32 v54, v54, v130
	v_add_f32_e32 v180, 0, v50
	v_exp_f32_e32 v54, v54
	v_sub_f32_e32 v55, v55, v130
	v_add_f32_e32 v180, v51, v180
	v_exp_f32_e32 v55, v55
	v_sub_f32_e32 v56, v56, v130
	v_add_f32_e32 v180, v52, v180
	v_exp_f32_e32 v56, v56
	v_sub_f32_e32 v57, v57, v130
	v_add_f32_e32 v180, v53, v180
	v_exp_f32_e32 v57, v57
	v_sub_f32_e32 v58, v58, v130
	v_add_f32_e32 v180, v54, v180
	v_exp_f32_e32 v58, v58
	v_sub_f32_e32 v59, v59, v130
	v_add_f32_e32 v180, v55, v180
	v_exp_f32_e32 v59, v59
	v_sub_f32_e32 v60, v60, v130
	v_add_f32_e32 v180, v56, v180
	v_exp_f32_e32 v60, v60
	v_sub_f32_e32 v61, v61, v130
	v_add_f32_e32 v180, v57, v180
	v_exp_f32_e32 v61, v61
	v_sub_f32_e32 v62, v62, v130
	v_add_f32_e32 v180, v58, v180
	v_exp_f32_e32 v62, v62
	v_sub_f32_e32 v63, v63, v130
	v_add_f32_e32 v180, v59, v180
	v_exp_f32_e32 v63, v63
	v_sub_f32_e32 v64, v64, v130
	v_add_f32_e32 v180, v60, v180
	v_exp_f32_e32 v64, v64
	v_sub_f32_e32 v65, v65, v130
	v_add_f32_e32 v180, v61, v180
	v_exp_f32_e32 v65, v65
	v_sub_f32_e32 v34, v34, v130
	v_add_f32_e32 v180, v62, v180
	v_exp_f32_e32 v181, v34
	v_sub_f32_e32 v34, v35, v130
	v_add_f32_e32 v180, v63, v180
	v_exp_f32_e32 v182, v34
	v_sub_f32_e32 v35, v36, v130
	v_add_f32_e32 v34, v64, v180
	v_exp_f32_e32 v180, v35
	v_sub_f32_e32 v35, v37, v130
	v_add_f32_e32 v34, v65, v34
	v_exp_f32_e32 v183, v35
	v_sub_f32_e32 v35, v38, v130
	v_add_f32_e32 v34, v181, v34
	v_exp_f32_e32 v184, v35
	v_sub_f32_e32 v35, v39, v130
	v_add_f32_e32 v34, v182, v34
	v_exp_f32_e32 v39, v35
	v_add_f32_e32 v34, v180, v34
	v_sub_f32_e32 v179, v179, v130
	v_add_f32_e32 v34, v183, v34
	v_add_f32_e32 v34, v184, v34
	v_exp_f32_e32 v38, v179
	v_add_f32_e32 v185, v39, v34
	v_sub_f32_e32 v34, v40, v130
	v_exp_f32_e32 v40, v34
	v_sub_f32_e32 v34, v41, v130
	v_exp_f32_e32 v41, v34
	v_sub_f32_e32 v34, v42, v130
	v_exp_f32_e32 v42, v34
	v_mul_f32_e32 v32, v38, v32
	v_mul_f32_e32 v33, v38, v33
	v_mul_f32_e32 v30, v38, v30
	v_mul_f32_e32 v31, v38, v31
	v_mul_f32_e32 v28, v38, v28
	v_mul_f32_e32 v29, v38, v29
	v_mul_f32_e32 v26, v38, v26
	v_mul_f32_e32 v27, v38, v27
	v_mul_f32_e32 v24, v38, v24
	v_mul_f32_e32 v25, v38, v25
	v_mul_f32_e32 v22, v38, v22
	v_mul_f32_e32 v23, v38, v23
	v_mul_f32_e32 v20, v38, v20
	v_mul_f32_e32 v21, v38, v21
	v_mul_f32_e32 v18, v38, v18
	v_mul_f32_e32 v19, v38, v19
	v_mul_f32_e32 v16, v38, v16
	v_mul_f32_e32 v17, v38, v17
	v_cvt_pk_bf16_f32 v34, v50, v51
	v_cvt_pk_bf16_f32 v35, v52, v53
	v_cvt_pk_bf16_f32 v36, v54, v55
	v_cvt_pk_bf16_f32 v37, v56, v57
	v_mul_f32_e32 v14, v38, v14
	v_mul_f32_e32 v15, v38, v15
	v_mul_f32_e32 v12, v38, v12
	v_mul_f32_e32 v13, v38, v13
	v_mul_f32_e32 v10, v38, v10
	v_mul_f32_e32 v11, v38, v11
	v_mul_f32_e32 v8, v38, v8
	v_mul_f32_e32 v9, v38, v9
	v_mul_f32_e32 v6, v38, v6
	v_mul_f32_e32 v7, v38, v7
	v_mul_f32_e32 v4, v38, v4
	v_mul_f32_e32 v5, v38, v5
	v_mul_f32_e32 v2, v38, v2
	v_mul_f32_e32 v3, v38, v3
	s_waitcnt lgkmcnt(7)
	v_mfma_f32_32x32x16_bf16 v[18:33], v[152:155], v[34:37], v[18:33]
	v_sub_f32_e32 v43, v43, v130
	v_exp_f32_e32 v43, v43
	v_sub_f32_e32 v44, v44, v130
	v_exp_f32_e32 v44, v44
	v_sub_f32_e32 v45, v45, v130
	v_exp_f32_e32 v45, v45
	v_sub_f32_e32 v46, v46, v130
	s_waitcnt lgkmcnt(5)
	v_mfma_f32_32x32x16_bf16 v[2:17], v[148:151], v[34:37], v[2:17]
	v_add_f32_e32 v34, v40, v185
	v_add_f32_e32 v34, v41, v34
	v_add_f32_e32 v50, v42, v34
	v_cvt_pk_bf16_f32 v34, v58, v59
	v_cvt_pk_bf16_f32 v35, v60, v61
	v_cvt_pk_bf16_f32 v36, v62, v63
	v_cvt_pk_bf16_f32 v37, v64, v65
	v_add_f32_e32 v50, v43, v50
	s_add_i32 s28, s28, 1
	v_mfma_f32_32x32x16_bf16 v[18:33], v[144:147], v[34:37], v[18:33]
	s_cmp_ge_i32 s28, s26
	s_waitcnt lgkmcnt(4)
	v_mfma_f32_32x32x16_bf16 v[2:17], v[140:143], v[34:37], v[2:17]
	v_add_f32_e32 v34, v44, v50
	v_add_f32_e32 v50, v45, v34
	v_cvt_pk_bf16_f32 v34, v181, v182
	v_cvt_pk_bf16_f32 v35, v180, v183
	v_cvt_pk_bf16_f32 v36, v184, v39
	v_cvt_pk_bf16_f32 v37, v40, v41
	v_exp_f32_e32 v39, v46
	v_sub_f32_e32 v40, v47, v130
	s_waitcnt lgkmcnt(3)
	v_mfma_f32_32x32x16_bf16 v[18:33], v[136:139], v[34:37], v[18:33]
	v_exp_f32_e32 v40, v40
	v_sub_f32_e32 v41, v48, v130
	v_exp_f32_e32 v41, v41
	v_add_f32_e32 v46, v39, v50
	v_add_f32_e32 v46, v40, v46
	v_add_f32_e32 v46, v41, v46
	s_waitcnt lgkmcnt(2)
	v_mfma_f32_32x32x16_bf16 v[2:17], v[132:135], v[34:37], v[2:17]
	v_sub_f32_e32 v34, v49, v130
	v_exp_f32_e32 v47, v34
	v_cvt_pk_bf16_f32 v34, v42, v43
	v_cvt_pk_bf16_f32 v35, v44, v45
	v_cvt_pk_bf16_f32 v36, v39, v40
	v_cvt_pk_bf16_f32 v37, v41, v47
	v_add_f32_e32 v39, v47, v46
	v_mov_b32_e32 v40, v39
	s_waitcnt lgkmcnt(1)
	v_mfma_f32_32x32x16_bf16 v[18:33], v[126:129], v[34:37], v[18:33]
	v_mov_b32_e32 v41, v39
	s_nop 1
	v_permlane32_swap_b32_e32 v40, v41
	v_cndmask_b32_e64 v40, v40, v41, s[2:3]
	v_add_f32_e32 v42, v39, v40
	v_fmac_f32_e32 v42, v165, v38
	v_mov_b64_e32 v[38:39], v[78:79]
	s_waitcnt lgkmcnt(0)
	v_mfma_f32_32x32x16_bf16 v[2:17], v[122:125], v[34:37], v[2:17]
	v_mov_b64_e32 v[34:35], v[66:67]
	v_mov_b64_e32 v[36:37], v[68:69]
	v_mov_b64_e32 v[40:41], v[80:81]
	s_waitcnt vmcnt(2)
	s_bitcmp1_b32 s101, 0
	s_cbranch_scc1 .Lattn_rot_odd
	v_mov_b64_e32 v[66:67], v[90:91]
	v_mov_b64_e32 v[78:79], v[94:95]
	v_mov_b64_e32 v[68:69], v[92:93]
	v_mov_b64_e32 v[80:81], v[96:97]
	s_branch .Lattn_rot_join

.LBB0_769:
	s_bitcmp1_b32 s68, 0
	s_cselect_b32 s8, 0x12000, 0
	v_add_u32_e32 v190, s8, v136
	ds_read_b128 v[98:101], v190
	ds_read_b128 v[138:141], v190 offset:1024
	ds_read_b128 v[102:105], v190 offset:16384
	ds_read_b128 v[142:145], v190 offset:17408
	ds_read_b128 v[146:149], v190 offset:8192
	ds_read_b128 v[150:153], v190 offset:9216
	ds_read_b128 v[154:157], v190 offset:24576
	ds_read_b128 v[158:161], v190 offset:25600
	v_add_u32_e32 v191, s49, v190
	ds_read_b128 v[162:165], v190 offset:2048
	ds_read_b128 v[166:169], v190 offset:3072
	ds_read_b128 v[170:173], v190 offset:18432
	ds_read_b128 v[174:177], v190 offset:19456
	ds_read_b128 v[178:181], v190 offset:10240
	ds_read_b128 v[182:185], v190 offset:11264
	ds_read_b128 v[186:189], v190 offset:26624
	ds_read_b128 v[198:201], v190 offset:27648
	v_cvt_pk_bf16_f32 v202, v2, v3
	v_cvt_pk_bf16_f32 v203, v4, v5
	v_cvt_pk_bf16_f32 v204, v6, v7
	v_cvt_pk_bf16_f32 v205, v8, v9
	s_waitcnt lgkmcnt(8)
	s_nop 0
	v_mfma_f32_32x32x16_bf16 v[114:129], v[98:101], v[202:205], 0
	v_mfma_f32_32x32x16_bf16 v[82:97], v[102:105], v[202:205], 0
	v_mfma_f32_32x32x16_bf16 v[98:113], v[146:149], v[202:205], 0
	v_cvt_pk_bf16_f32 v146, v10, v11
	v_cvt_pk_bf16_f32 v147, v12, v13
	v_cvt_pk_bf16_f32 v148, v14, v15
	v_cvt_pk_bf16_f32 v149, v16, v17
	v_mfma_f32_32x32x16_bf16 v[66:81], v[154:157], v[202:205], 0
	s_nop 0
	v_mfma_f32_32x32x16_bf16 v[82:97], v[142:145], v[146:149], v[82:97]
	v_mfma_f32_32x32x16_bf16 v[66:81], v[158:161], v[146:149], v[66:81]
	v_mfma_f32_32x32x16_bf16 v[114:129], v[138:141], v[146:149], v[114:129]
	v_mfma_f32_32x32x16_bf16 v[98:113], v[150:153], v[146:149], v[98:113]
	ds_read_b128 v[138:141], v190 offset:4096
	ds_read_b128 v[142:145], v190 offset:5120
	ds_read_b128 v[146:149], v190 offset:20480
	ds_read_b128 v[150:153], v190 offset:21504
	ds_read_b128 v[154:157], v190 offset:12288
	ds_read_b128 v[158:161], v190 offset:13312
	ds_read_b128 v[202:205], v190 offset:28672
	ds_read_b128 v[206:209], v190 offset:29696
	v_cvt_pk_bf16_f32 v210, v18, v19
	v_cvt_pk_bf16_f32 v211, v20, v21
	v_cvt_pk_bf16_f32 v212, v22, v23
	v_cvt_pk_bf16_f32 v213, v24, v25
	s_waitcnt lgkmcnt(8)
	s_nop 0
	v_mfma_f32_32x32x16_bf16 v[82:97], v[170:173], v[210:213], v[82:97]
	v_mfma_f32_32x32x16_bf16 v[66:81], v[186:189], v[210:213], v[66:81]
	v_mfma_f32_32x32x16_bf16 v[114:129], v[162:165], v[210:213], v[114:129]
	v_cvt_pk_bf16_f32 v162, v26, v27
	v_cvt_pk_bf16_f32 v163, v28, v29
	v_cvt_pk_bf16_f32 v164, v30, v31
	v_cvt_pk_bf16_f32 v165, v32, v33
	v_mfma_f32_32x32x16_bf16 v[98:113], v[178:181], v[210:213], v[98:113]
	s_nop 0
	v_mfma_f32_32x32x16_bf16 v[82:97], v[174:177], v[162:165], v[82:97]
	v_mfma_f32_32x32x16_bf16 v[66:81], v[198:201], v[162:165], v[66:81]
	v_mfma_f32_32x32x16_bf16 v[114:129], v[166:169], v[162:165], v[114:129]
	v_mfma_f32_32x32x16_bf16 v[98:113], v[182:185], v[162:165], v[98:113]
	ds_read_b128 v[162:165], v190 offset:6144
	ds_read_b128 v[166:169], v190 offset:7168
	ds_read_b128 v[170:173], v190 offset:22528
	ds_read_b128 v[174:177], v190 offset:23552
	ds_read_b128 v[178:181], v190 offset:14336
	ds_read_b128 v[182:185], v190 offset:15360
	ds_read_b128 v[186:189], v190 offset:30720
	ds_read_b128 v[198:201], v190 offset:31744
	v_cvt_pk_bf16_f32 v210, v34, v35
	v_cvt_pk_bf16_f32 v211, v36, v37
	v_cvt_pk_bf16_f32 v212, v38, v39
	v_cvt_pk_bf16_f32 v213, v40, v41
	s_waitcnt lgkmcnt(8)
	s_nop 0
	v_mfma_f32_32x32x16_bf16 v[82:97], v[146:149], v[210:213], v[82:97]
	v_mfma_f32_32x32x16_bf16 v[66:81], v[202:205], v[210:213], v[66:81]
	v_mfma_f32_32x32x16_bf16 v[114:129], v[138:141], v[210:213], v[114:129]
	v_cvt_pk_bf16_f32 v138, v42, v43
	v_cvt_pk_bf16_f32 v139, v44, v45
	v_cvt_pk_bf16_f32 v140, v46, v47
	v_cvt_pk_bf16_f32 v141, v48, v49
	v_mfma_f32_32x32x16_bf16 v[98:113], v[154:157], v[210:213], v[98:113]
	s_nop 0
	v_mfma_f32_32x32x16_bf16 v[82:97], v[150:153], v[138:141], v[82:97]
	v_mfma_f32_32x32x16_bf16 v[66:81], v[206:209], v[138:141], v[66:81]
	v_mfma_f32_32x32x16_bf16 v[114:129], v[142:145], v[138:141], v[114:129]
	v_mfma_f32_32x32x16_bf16 v[98:113], v[158:161], v[138:141], v[98:113]
	s_barrier
	ds_read_b128 v[138:141], v191 offset:57344
	ds_read_b128 v[142:145], v191 offset:58368
	ds_read_b128 v[146:149], v191 offset:59392
	ds_read_b128 v[150:153], v191 offset:60416
	ds_read_b128 v[154:157], v191 offset:61440
	ds_read_b128 v[158:161], v191 offset:62464
	ds_read_b128 v[202:205], v191 offset:63488
	ds_read_b128 v[206:209], v191 offset:64512
	v_cvt_pk_bf16_f32 v210, v50, v51
	v_cvt_pk_bf16_f32 v211, v52, v53
	v_cvt_pk_bf16_f32 v212, v54, v55
	v_cvt_pk_bf16_f32 v213, v56, v57
	s_waitcnt lgkmcnt(8)
	s_nop 0
	v_mfma_f32_32x32x16_bf16 v[82:97], v[170:173], v[210:213], v[82:97]
	v_mfma_f32_32x32x16_bf16 v[66:81], v[186:189], v[210:213], v[66:81]
	v_mfma_f32_32x32x16_bf16 v[114:129], v[162:165], v[210:213], v[114:129]
	v_cvt_pk_bf16_f32 v162, v58, v59
	v_cvt_pk_bf16_f32 v163, v60, v61
	v_cvt_pk_bf16_f32 v164, v62, v63
	v_cvt_pk_bf16_f32 v165, v64, v65
	v_mfma_f32_32x32x16_bf16 v[98:113], v[178:181], v[210:213], v[98:113]
	s_nop 0
	v_mfma_f32_32x32x16_bf16 v[82:97], v[174:177], v[162:165], v[82:97]
	v_mfma_f32_32x32x16_bf16 v[66:81], v[198:201], v[162:165], v[66:81]
	v_mfma_f32_32x32x16_bf16 v[114:129], v[166:169], v[162:165], v[114:129]
	v_mfma_f32_32x32x16_bf16 v[98:113], v[182:185], v[162:165], v[98:113]
	ds_read_b128 v[162:165], v190 offset:32768
	ds_read_b128 v[166:169], v190 offset:33792
	ds_read_b128 v[170:173], v190 offset:34816
	ds_read_b128 v[174:177], v190 offset:35840
	ds_read_b128 v[178:181], v190 offset:36864
	ds_read_b128 v[182:185], v190 offset:37888
	ds_read_b128 v[186:189], v190 offset:38912
	ds_read_b128 v[198:201], v190 offset:39936
	s_waitcnt lgkmcnt(8)
	s_nop 1
	v_sub_f32_e32 v114, v138, v114
	v_sub_f32_e32 v115, v139, v115
	v_sub_f32_e32 v116, v140, v116
	v_sub_f32_e32 v117, v141, v117
	v_sub_f32_e32 v118, v142, v118
	v_sub_f32_e32 v119, v143, v119
	v_sub_f32_e32 v122, v146, v122
	v_sub_f32_e32 v123, v147, v123
	v_sub_f32_e32 v120, v144, v120
	v_sub_f32_e32 v121, v145, v121
	v_sub_f32_e32 v124, v148, v124
	v_sub_f32_e32 v125, v149, v125
	v_sub_f32_e32 v126, v150, v126
	v_sub_f32_e32 v127, v151, v127
	v_cvt_pk_bf16_f32 v114, v114, v115
	v_cvt_pk_bf16_f32 v115, v116, v117
	v_cvt_pk_bf16_f32 v116, v118, v119
	v_cvt_pk_bf16_f32 v118, v122, v123
	v_sub_f32_e32 v122, v152, v128
	v_sub_f32_e32 v123, v153, v129
	v_sub_f32_e32 v98, v154, v98
	v_sub_f32_e32 v99, v155, v99
	v_sub_f32_e32 v100, v156, v100
	v_sub_f32_e32 v101, v157, v101
	v_sub_f32_e32 v102, v158, v102
	v_sub_f32_e32 v103, v159, v103
	v_sub_f32_e32 v104, v160, v104
	v_sub_f32_e32 v105, v161, v105
	v_sub_f32_e32 v106, v202, v106
	v_sub_f32_e32 v107, v203, v107
	v_sub_f32_e32 v108, v204, v108
	v_sub_f32_e32 v109, v205, v109
	v_sub_f32_e32 v110, v206, v110
	v_sub_f32_e32 v111, v207, v111
	v_sub_f32_e32 v113, v209, v113
	v_sub_f32_e32 v112, v208, v112
	v_cvt_pk_bf16_f32 v117, v120, v121
	v_cvt_pk_bf16_f32 v119, v124, v125
	v_cvt_pk_bf16_f32 v120, v126, v127
	v_cvt_pk_bf16_f32 v121, v122, v123
	v_cvt_pk_bf16_f32 v98, v98, v99
	v_cvt_pk_bf16_f32 v99, v100, v101
	v_cvt_pk_bf16_f32 v100, v102, v103
	v_cvt_pk_bf16_f32 v101, v104, v105
	v_cvt_pk_bf16_f32 v102, v106, v107
	v_cvt_pk_bf16_f32 v103, v108, v109
	v_cvt_pk_bf16_f32 v104, v110, v111
	v_cvt_pk_bf16_f32 v105, v112, v113
	ds_read_b128 v[106:109], v190 offset:40960
	ds_read_b128 v[110:113], v190 offset:41984
	ds_read_b128 v[122:125], v190 offset:43008
	ds_read_b128 v[126:129], v190 offset:44032
	ds_read_b128 v[138:141], v190 offset:45056
	ds_read_b128 v[142:145], v190 offset:46080
	ds_read_b128 v[146:149], v190 offset:47104
	ds_read_b128 v[150:153], v190 offset:48128
	s_waitcnt lgkmcnt(8)
	v_mfma_f32_32x32x16_bf16 v[82:97], v[162:165], v[114:117], v[82:97]
	v_mfma_f32_32x32x16_bf16 v[66:81], v[178:181], v[114:117], v[66:81]
	v_mfma_f32_32x32x16_bf16 v[82:97], v[166:169], v[118:121], v[82:97]
	v_mfma_f32_32x32x16_bf16 v[66:81], v[182:185], v[118:121], v[66:81]
	v_mfma_f32_32x32x16_bf16 v[82:97], v[170:173], v[98:101], v[82:97]
	v_mfma_f32_32x32x16_bf16 v[66:81], v[186:189], v[98:101], v[66:81]
	v_mfma_f32_32x32x16_bf16 v[82:97], v[174:177], v[102:105], v[82:97]
	v_mfma_f32_32x32x16_bf16 v[66:81], v[198:201], v[102:105], v[66:81]
	ds_read_b128 v[154:157], v190 offset:49152
	ds_read_b128 v[158:161], v190 offset:50176
	ds_read_b128 v[162:165], v190 offset:51200
	ds_read_b128 v[166:169], v190 offset:52224
	ds_read_b128 v[170:173], v190 offset:53248
	ds_read_b128 v[174:177], v190 offset:54272
	ds_read_b128 v[178:181], v190 offset:55296
	ds_read_b128 v[182:185], v190 offset:56320
	v_mul_f32_e32 v16, v134, v16
	v_mul_f32_e32 v17, v134, v17
	v_mul_f32_e32 v14, v134, v14
	v_mul_f32_e32 v15, v134, v15
	v_mul_f32_e32 v12, v134, v12
	v_mul_f32_e32 v13, v134, v13
	v_mul_f32_e32 v10, v134, v10
	v_mul_f32_e32 v11, v134, v11
	v_mul_f32_e32 v8, v134, v8
	v_mul_f32_e32 v9, v134, v9
	v_mul_f32_e32 v6, v134, v6
	v_mul_f32_e32 v7, v134, v7
	v_mul_f32_e32 v4, v134, v4
	v_mul_f32_e32 v5, v134, v5
	v_mul_f32_e32 v2, v134, v2
	v_mul_f32_e32 v3, v134, v3
	v_mul_f32_e32 v32, v134, v32
	v_mul_f32_e32 v33, v134, v33
	v_mul_f32_e32 v30, v134, v30
	v_mul_f32_e32 v31, v134, v31
	v_mul_f32_e32 v28, v134, v28
	v_mul_f32_e32 v29, v134, v29
	v_mul_f32_e32 v26, v134, v26
	v_mul_f32_e32 v27, v134, v27
	v_mul_f32_e32 v24, v134, v24
	v_mul_f32_e32 v25, v134, v25
	v_mul_f32_e32 v22, v134, v22
	v_mul_f32_e32 v23, v134, v23
	v_mul_f32_e32 v20, v134, v20
	v_mul_f32_e32 v21, v134, v21
	v_mul_f32_e32 v18, v134, v18
	v_mul_f32_e32 v19, v134, v19
	s_waitcnt lgkmcnt(8)
	v_mfma_f32_32x32x16_bf16 v[2:17], v[106:109], v[114:117], v[2:17]
	v_mfma_f32_32x32x16_bf16 v[18:33], v[138:141], v[114:117], v[18:33]
	v_mfma_f32_32x32x16_bf16 v[2:17], v[110:113], v[118:121], v[2:17]
	v_mfma_f32_32x32x16_bf16 v[18:33], v[142:145], v[118:121], v[18:33]
	v_mfma_f32_32x32x16_bf16 v[2:17], v[122:125], v[98:101], v[2:17]
	v_mfma_f32_32x32x16_bf16 v[18:33], v[146:149], v[98:101], v[18:33]
	v_mfma_f32_32x32x16_bf16 v[2:17], v[126:129], v[102:105], v[2:17]
	v_mfma_f32_32x32x16_bf16 v[18:33], v[150:153], v[102:105], v[18:33]
	v_mul_f32_e64 v48, v48, v134
	v_mul_f32_e64 v49, v49, v134
	v_mul_f32_e64 v46, v46, v134
	v_mul_f32_e64 v47, v47, v134
	v_mul_f32_e64 v44, v44, v134
	v_mul_f32_e64 v45, v45, v134
	v_mul_f32_e32 v42, v134, v42
	v_mul_f32_e32 v43, v134, v43
	v_mul_f32_e32 v40, v134, v40
	v_mul_f32_e32 v41, v134, v41
	v_mul_f32_e32 v38, v134, v38
	v_mul_f32_e32 v39, v134, v39
	v_mul_f32_e32 v36, v134, v36
	v_mul_f32_e32 v37, v134, v37
	v_mul_f32_e32 v34, v134, v34
	v_mul_f32_e32 v35, v134, v35
	v_mul_f32_e32 v64, v134, v64
	v_mul_f32_e32 v65, v134, v65
	v_mul_f32_e32 v62, v134, v62
	v_mul_f32_e32 v63, v134, v63
	v_mul_f32_e32 v60, v134, v60
	v_mul_f32_e32 v61, v134, v61
	v_mul_f32_e32 v58, v134, v58
	v_mul_f32_e32 v59, v134, v59
	v_mul_f32_e32 v56, v134, v56
	v_mul_f32_e32 v57, v134, v57
	v_mul_f32_e32 v54, v134, v54
	v_mul_f32_e32 v55, v134, v55
	v_mul_f32_e32 v52, v134, v52
	v_mul_f32_e32 v53, v134, v53
	v_mul_f32_e32 v50, v134, v50
	v_mul_f32_e32 v51, v134, v51
	s_waitcnt lgkmcnt(0)
	v_mfma_f32_32x32x16_bf16 v[34:49], v[154:157], v[114:117], v[34:49]
	s_mov_b64 s[8:9], -1
	s_cmpk_gt_i32 s10, 0xff
	v_mfma_f32_32x32x16_bf16 v[50:65], v[170:173], v[114:117], v[50:65]
	v_mfma_f32_32x32x16_bf16 v[34:49], v[158:161], v[118:121], v[34:49]
	v_mfma_f32_32x32x16_bf16 v[50:65], v[174:177], v[118:121], v[50:65]
	v_mfma_f32_32x32x16_bf16 v[34:49], v[162:165], v[98:101], v[34:49]
	v_mfma_f32_32x32x16_bf16 v[50:65], v[178:181], v[98:101], v[50:65]
	v_mfma_f32_32x32x16_bf16 v[34:49], v[166:169], v[102:105], v[34:49]
	v_mfma_f32_32x32x16_bf16 v[50:65], v[182:185], v[102:105], v[50:65]
	s_cbranch_scc0 .LBB0_771
	s_lshl_b32 s11, s10, 6
	s_mov_b64 s[8:9], 0
